# g17: g13 + w_out weight transposition moved from P0 to the idle tail of the P3 converter workgroups
# speedup vs baseline: 1.0061x; 1.0061x over previous
.LBB0_10:
	s_add_i32 s40, s40, s8
	s_add_i32 s16, s16, s17
	s_add_i32 s18, s18, s19
	s_cmpk_gt_i32 s40, 0x15ff
	s_cbranch_scc1 .LBB0_15

.LBB0_205:
	s_mov_b32 s98, 0
	s_cmp_lt_i32 s60, 4
	s_cselect_b64 s[0:1], -1, 0
	s_and_b64 s[34:35], s[0:1], s[4:5]
	s_mov_b64 s[0:1], s[60:61]
	v_writelane_b32 v254, s0, 34
	s_andn2_b64 vcc, exec, s[34:35]
	s_nop 0
	v_writelane_b32 v254, s1, 35
	v_writelane_b32 v254, s2, 36
	v_writelane_b32 v254, s3, 37
	s_cbranch_vccnz .LBB0_320
	s_and_b32 s0, s33, 15
	s_cmp_lg_u32 s0, 0
	s_cbranch_scc0 .LBB0_286
	v_readlane_b32 s0, v254, 0
	s_and_b32 s4, s0, 1
	v_readlane_b32 s1, v254, 1
	s_ashr_i32 s71, s0, 1
	s_xor_b32 s0, s4, 1
	s_add_i32 s5, s33, s0
	s_cbranch_execnz .LBB0_209

.LBB0_209:
	s_mov_b32 s98, s4
	s_mov_b32 s99, s71
	s_cmp_lg_u32 s4, 0
	s_cbranch_scc1 .LBB0_288
	v_writelane_b32 v254, s34, 38
	s_cmpk_gt_i32 s71, 0xff
	s_nop 0
	v_writelane_b32 v254, s35, 39
	v_writelane_b32 v254, s80, 40
	s_nop 1
	v_writelane_b32 v254, s81, 41
	v_writelane_b32 v254, s84, 42
	s_nop 1
	v_writelane_b32 v254, s85, 43
	v_writelane_b32 v254, s86, 44
	v_writelane_b32 v254, s87, 45
	s_cbranch_scc1 .LBB0_287
	s_ashr_i32 s0, s5, 1
	v_writelane_b32 v254, s0, 46
	s_add_u32 s0, s96, 0x98a00000
	v_writelane_b32 v254, s0, 47
	s_addc_u32 s0, s97, 0
	s_add_u32 s50, s96, 0x4e000000
	s_addc_u32 s51, s97, 0
	v_bfe_u32 v2, v0, 3, 1
	v_lshrrev_b32_e32 v3, 5, v186
	s_add_u32 s52, s96, 0x38000000
	v_xor_b32_e32 v4, v2, v3
	s_addc_u32 s53, s97, 0
	s_lshl_b32 s1, s82, 1
	v_lshrrev_b32_e32 v5, 4, v186
	v_lshlrev_b32_e32 v11, 4, v4
	v_bitop3_b32 v4, v3, v2, 2 bitop3:0x36
	s_lshl_b32 s85, s82, 4
	s_and_b32 s1, s1, 2
	v_writelane_b32 v254, s0, 48
	v_xor_b32_e32 v6, v2, v5
	v_bitop3_b32 v7, v2, v5, 2 bitop3:0x36
	v_lshlrev_b32_e32 v12, 4, v4
	v_bitop3_b32 v4, v2, v3, 2 bitop3:0x36
	v_bitop3_b32 v3, v2, v3, 2 bitop3:0x14
	v_bitop3_b32 v2, s1, v5, v2 bitop3:0x36
	s_add_u32 s1, s96, 0x4e400000
	v_writelane_b32 v254, s1, 49
	s_addc_u32 s1, s97, 0
	v_writelane_b32 v254, s1, 50
	v_lshlrev_b32_e32 v17, 4, v2
	v_lshlrev_b32_e32 v2, 4, v0
	v_cmp_gt_u32_e64 s[4:5], 64, v0
	s_cmp_lt_u32 s3, 64
	v_and_b32_e32 v1, 15, v0
	v_lshlrev_b32_e32 v13, 4, v4
	v_writelane_b32 v254, s4, 51
	s_cselect_b64 s[66:67], -1, 0
	v_and_b32_e32 v106, 0xf0, v2
	v_mov_b32_e32 v107, 0
	v_or_b32_e32 v4, 0x200, v0
	v_lshlrev_b32_e32 v28, 3, v186
	s_add_i32 s18, 0, 0x22000
	v_lshlrev_b32_e32 v14, 4, v3
	v_and_b32_e32 v152, 48, v2
	v_writelane_b32 v254, s5, 52
	v_lshl_add_u64 v[2:3], s[96:97], 0, v[106:107]
	s_mov_b64 s[4:5], 0x98a01400
	v_lshrrev_b32_e32 v19, 3, v0
	v_lshrrev_b32_e32 v20, 3, v4
	v_lshlrev_b32_e32 v23, 3, v1
	v_add_u32_e32 v158, s18, v28
	s_add_i32 s18, 0, 0x22200
	s_movk_i32 s0, 0x110
	v_or_b32_e32 v15, s85, v1
	v_lshlrev_b32_e32 v18, 3, v0
	v_lshl_add_u64 v[108:109], v[2:3], 0, s[4:5]
	s_mov_b64 s[4:5], 0x98a01000
	v_and_b32_e32 v112, 62, v19
	v_and_b32_e32 v114, 0x7e, v20
	v_lshrrev_b32_e32 v21, 2, v0
	v_or_b32_e32 v25, 1, v19
	v_xor_b32_e32 v19, v23, v19
	v_add_u32_e32 v159, s18, v28
	s_add_i32 s18, 0, 0x22400
	v_or_b32_e32 v31, 1, v20
	v_xor_b32_e32 v20, v20, v23
	v_lshlrev_b32_e32 v8, 3, v5
	v_mul_lo_u32 v16, v15, s0
	v_lshl_add_u64 v[110:111], v[2:3], 0, s[4:5]
	v_and_b32_e32 v4, 56, v18
	s_add_i32 s4, 0, 0x22800
	v_lshlrev_b32_e32 v19, 1, v19
	s_add_i32 s5, 0, 0x11000
	v_add_u32_e32 v160, s18, v28
	s_add_i32 s18, 0, 0x22600
	v_lshlrev_b32_e32 v20, 1, v20
	v_bitop3_b32 v18, v18, v21, 56 bitop3:0x6c
	v_lshlrev_b32_e32 v166, 2, v5
	v_mul_u32_u24_e32 v113, 0x110, v1
	v_and_b32_e32 v10, 8, v8
	v_lshl_add_u32 v154, v112, 2, s4
	v_and_b32_e32 v19, 0xf0, v19
	v_and_b32_e32 v26, 12, v21
	v_add_u32_e32 v161, s18, v28
	v_add_u32_e32 v162, s4, v28
	v_lshl_add_u32 v163, v114, 2, s4
	v_and_b32_e32 v20, 0xf0, v20
	v_lshlrev_b32_e32 v18, 1, v18
	s_lshl_b32 s4, s82, 5
	s_add_i32 s18, 0, 0x1dc00
	v_add_u32_e32 v33, 0, v16
	v_add3_u32 v168, s5, v16, v17
	v_or_b32_e32 v16, s85, v166
	v_or_b32_e32 v9, v10, v113
	v_add3_u32 v19, s5, v19, v26
	s_add_i32 s26, 0, 0x19800
	v_add3_u32 v20, s5, v20, v26
	v_lshrrev_b32_e32 v23, 1, v0
	v_mul_u32_u24_e32 v26, 0x110, v4
	v_and_b32_e32 v18, 0xf0, v18
	s_add_i32 s19, s4, s18
	v_lshl_add_u32 v169, v16, 1, s18
	v_or_b32_e32 v16, 2, v166
	s_movk_i32 s1, 0xf0
	v_and_b32_e32 v116, 0x7e, v21
	v_and_b32_e32 v21, 12, v23
	v_add3_u32 v18, s26, v18, v26
	v_add_u32_e32 v164, s19, v8
	v_or_b32_e32 v23, 16, v1
	v_mov_b32_e32 v26, 0x1100
	v_or_b32_e32 v8, s4, v8
	v_cmp_gt_u32_e64 s[22:23], v16, v1
	v_or_b32_e32 v16, 3, v166
	v_add3_u32 v170, s26, v11, v9
	v_add3_u32 v171, s26, v12, v9
	v_add3_u32 v172, s26, v13, v9
	v_add3_u32 v173, s26, v14, v9
	v_lshlrev_b32_e32 v9, 1, v1
	v_mul_u32_u24_e32 v165, 0x110, v23
	v_mad_u32_u24 v26, v23, s0, v26
	v_cmp_gt_u32_e64 s[24:25], v16, v1
	v_bitop3_b32 v16, v8, s1, v9 bitop3:0x48
	v_lshlrev_b32_e32 v23, 1, v23
	v_or_b32_e32 v36, 64, v9
	v_or_b32_e32 v9, 0x60, v9
	v_bitop3_b32 v23, v8, s1, v23 bitop3:0x48
	v_bitop3_b32 v36, v8, s1, v36 bitop3:0x48
	v_bitop3_b32 v8, v8, s1, v9 bitop3:0x48
	s_movk_i32 s27, 0x1100
	s_mul_i32 s19, s82, 0x1100
	v_add_u32_e32 v8, s26, v8
	s_add_i32 s28, s19, 0
	v_add3_u32 v36, s26, v36, v26
	v_add3_u32 v26, v26, v8, s27
	v_and_b32_e32 v8, 3, v0
	v_lshrrev_b32_e32 v153, 2, v186
	v_lshl_add_u32 v37, v6, 4, s26
	v_mov_b32_e32 v6, s28
	v_lshlrev_b32_e32 v106, 5, v8
	v_add3_u32 v27, s26, v113, v10
	v_add3_u32 v23, s26, v23, v165
	s_and_b32 s94, s4, 0x7fffffc0
	v_lshl_add_u32 v7, v7, 4, s26
	v_mad_u32_u24 v38, v153, s0, v6
	v_lshlrev_b32_e32 v174, 6, v8
	v_cmp_eq_u32_e64 s[26:27], 0, v8
	v_lshlrev_b32_e32 v6, 4, v8
	v_lshl_add_u64 v[8:9], s[96:97], 0, v[106:107]
	s_mov_b64 s[4:5], 0x4e800000
	s_lshr_b32 s1, s3, 8
	v_lshl_add_u64 v[118:119], v[8:9], 0, s[4:5]
	s_mulk_i32 s1, 0xc00
	s_lshl_b32 s4, s82, 7
	s_add_i32 s1, s1, 0
	s_and_b32 s4, s4, 0x180
	s_add_i32 s1, s1, s4
	s_add_i32 s6, 0, 0x23a40
	s_xor_b32 s95, s94, 64
	s_xor_b32 s86, s94, 0x80
	s_xor_b32 s83, s94, 0xc0
	s_add_i32 s1, s1, 0x22400
	s_add_u32 s4, s96, 0x38003800
	v_writelane_b32 v254, s4, 53
	s_addc_u32 s4, s97, 0
	v_writelane_b32 v254, s4, 54
	s_mov_b64 s[4:5], 0x38002800
	v_lshl_add_u64 v[120:121], v[2:3], 0, s[4:5]
	s_mov_b64 s[4:5], 0x38003000
	v_lshl_add_u64 v[122:123], v[2:3], 0, s[4:5]
	v_mad_u32_u24 v3, v1, s0, v14
	v_or_b32_e32 v3, v3, v10
	s_add_i32 s4, 0, 0x22a00
	v_add_u32_e32 v182, 0x1a900, v3
	v_mad_u32_u24 v3, v1, s0, v13
	v_lshlrev_b32_e32 v34, 2, v1
	v_add_u32_e32 v175, s4, v28
	s_add_i32 s4, 0, 0x23800
	v_and_b32_e32 v179, 48, v186
	v_or_b32_e32 v3, v3, v10
	v_lshl_add_u32 v177, v186, 2, s1
	v_add_u32_e32 v178, s1, v34
	v_add_u32_e32 v180, s1, v179
	s_add_u32 s1, s96, 0x4e600000
	v_add_u32_e32 v183, 0x1a900, v3
	v_mad_u32_u24 v3, v1, s0, v12
	v_writelane_b32 v254, s1, 55
	s_addc_u32 s1, s97, 0
	v_or_b32_e32 v3, v3, v10
	v_writelane_b32 v254, s1, 56
	v_add_u32_e32 v184, 0x19800, v3
	v_mad_u32_u24 v3, v1, s0, v11
	s_add_i32 s0, 0, 0x23a00
	v_writelane_b32 v254, s0, 57
	v_lshlrev_b32_e32 v2, 5, v5
	v_writelane_b32 v254, s50, 58
	v_lshl_add_u32 v22, v1, 4, 0
	v_mul_u32_u24_e32 v24, 0x110, v112
	v_mul_u32_u24_e32 v25, 0x110, v25
	v_mul_u32_u24_e32 v29, 0x880, v1
	v_mul_u32_u24_e32 v30, 0x110, v114
	v_mul_u32_u24_e32 v31, 0x110, v31
	v_and_b32_e32 v32, 48, v0
	v_add_u32_e32 v35, s28, v34
	v_mul_u32_u24_e32 v17, 0x440, v5
	s_mov_b32 s1, 0x8800
	s_and_b32 s87, s82, 0x3fffffe
	v_or_b32_e32 v3, v3, v10
	v_add_u32_e32 v2, 0, v2
	v_writelane_b32 v254, s51, 59
	v_mov_b32_e32 v115, v107
	v_mov_b32_e32 v117, v107
	s_mov_b32 s69, 0
	v_or_b32_e32 v155, 0x2400, v152
	v_lshl_add_u32 v156, v0, 2, s6
	v_lshlrev_b32_e32 v157, 1, v186
	v_cmp_eq_u32_e64 s[6:7], 0, v186
	v_cmp_gt_u32_e64 s[8:9], 2, v186
	v_cmp_gt_u32_e64 s[10:11], 4, v186
	v_cmp_gt_u32_e64 s[12:13], 8, v186
	v_cmp_gt_u32_e64 s[14:15], 16, v186
	v_cmp_gt_u32_e64 s[16:17], 32, v186
	v_add_u32_e32 v167, s18, v32
	v_cmp_gt_u32_e64 s[18:19], v166, v1
	v_cmp_lt_u32_e64 s[20:21], v166, v1
	s_movk_i32 s3, 0xc00
	v_lshl_add_u32 v176, v15, 2, s4
	v_add3_u32 v181, v113, v32, s1
	s_add_i32 s87, s87, 2
	v_add_u32_e32 v185, 0x19800, v3
	s_movk_i32 s80, 0x5800
	s_mov_b32 s84, 0x7f800000
	s_movk_i32 s92, 0x1800
	v_lshlrev_b32_e32 v124, 1, v4
	s_mov_b32 s81, 0x800000
	s_mov_b32 s44, 0x3f317217
	s_mov_b32 s45, 0x41a00000
	s_mov_b32 s46, 0xffff0000
	v_add_u32_e32 v187, v27, v16
	v_add_u32_e32 v188, v23, v10
	v_add_u32_e32 v189, v36, v10
	v_add_u32_e32 v190, v26, v10
	s_mov_b32 s47, 0xbfb8aa3b
	s_mov_b32 s70, 0x3db504f3
	v_add_u32_e32 v191, 0x23800, v2
	v_lshlrev_b32_e32 v106, 1, v6
	v_mov_b32_e32 v192, 0x7f800000
	v_mbcnt_lo_u32_b32 v193, -1, 0
	v_mov_b32_e32 v194, 0x41b17218
	v_bfrev_b32_e32 v195, 0.5
	v_add_u32_e32 v196, v22, v24
	v_add_u32_e32 v197, v22, v25
	v_add_u32_e32 v198, v19, v29
	v_add_u32_e32 v199, v22, v30
	v_add_u32_e32 v200, v22, v31
	v_add_u32_e32 v201, v20, v29
	v_add_u32_e32 v202, v18, v21
	v_add_u32_e32 v203, v33, v32
	v_add_u32_e32 v204, v35, v17
	v_add_u32_e32 v205, v38, v174
	v_add_u32_e32 v206, v37, v113
	v_add_u32_e32 v207, v7, v113
	v_mov_b32_e32 v208, 0xff61b1e6
	v_writelane_b32 v254, s52, 60
	s_nop 1
	v_writelane_b32 v254, s53, 61
	s_branch .LBB0_213

.LBB0_320:
	s_cmp_eq_u32 s98, 1
	s_cbranch_scc0 .Lwo_skip
	v_writelane_b32 v253, s16, 0
	v_writelane_b32 v253, s17, 1
	v_writelane_b32 v253, s18, 2
	v_writelane_b32 v253, s19, 3
	v_writelane_b32 v253, s20, 4
	v_writelane_b32 v253, s21, 5
	v_writelane_b32 v253, s22, 6
	v_writelane_b32 v253, s23, 7
	v_writelane_b32 v253, s24, 8
	v_writelane_b32 v253, s25, 9
	v_writelane_b32 v253, s26, 10
	v_writelane_b32 v253, s27, 11
	v_writelane_b32 v253, s28, 12
	v_writelane_b32 v253, s29, 13
	v_writelane_b32 v253, s30, 14
	v_writelane_b32 v253, s31, 15
	v_writelane_b32 v253, s32, 16
	v_writelane_b32 v253, s33, 17
	v_writelane_b32 v253, s34, 18
	v_writelane_b32 v253, s35, 19
	v_writelane_b32 v253, s36, 20
	v_writelane_b32 v253, s37, 21
	v_writelane_b32 v253, s38, 22
	v_writelane_b32 v253, s39, 23
	v_writelane_b32 v253, s40, 24
	v_writelane_b32 v253, s41, 25
	s_lshl_b32 s6, s99, 3
	s_add_i32 s6, s6, s82
	s_addk_i32 s6, 0x1600
	s_movk_i32 s8, 0x400
	s_add_u32 s7, s96, 0x200000
	s_addc_u32 s9, s97, 0
	s_add_u32 s14, s96, 0x3000000
	s_mul_i32 s0, s82, 0x4200
	v_lshlrev_b32_e32 v2, 2, v0
	s_addc_u32 s15, s97, 0
	s_add_i32 s0, s0, 0
	v_lshrrev_b32_e32 v1, 3, v186
	v_and_b32_e32 v2, 28, v2
	v_lshlrev_b32_e32 v4, 3, v0
	v_lshl_add_u32 v38, v2, 2, s0
	v_mul_u32_u24_e32 v39, 0x84, v1
	v_and_b32_e32 v4, 0x78, v4
	v_lshrrev_b32_e32 v22, 4, v186
	v_mov_b32_e32 v3, 0
	v_mul_u32_u24_e32 v5, 0x84, v4
	v_lshlrev_b32_e32 v6, 2, v22
	v_or_b32_e32 v24, 4, v22
	v_or_b32_e32 v26, 8, v22
	v_or_b32_e32 v28, 12, v22
	v_or_b32_e32 v30, 16, v22
	v_or_b32_e32 v32, 20, v22
	v_or_b32_e32 v34, 24, v22
	v_or_b32_e32 v36, 28, v22
	v_add_u32_e32 v42, v38, v39
	s_mov_b32 s1, 0
	v_add3_u32 v5, s0, v5, v6
	v_lshlrev_b32_e32 v6, 13, v22
	v_mov_b32_e32 v7, v3
	v_lshlrev_b32_e32 v8, 13, v24
	v_mov_b32_e32 v9, v3
	v_lshlrev_b32_e32 v10, 13, v26
	v_mov_b32_e32 v11, v3
	v_lshlrev_b32_e32 v12, 13, v28
	v_mov_b32_e32 v13, v3
	v_lshlrev_b32_e32 v14, 13, v30
	v_mov_b32_e32 v15, v3
	v_lshlrev_b32_e32 v16, 13, v32
	v_mov_b32_e32 v17, v3
	v_lshlrev_b32_e32 v18, 13, v34
	v_mov_b32_e32 v19, v3
	v_lshlrev_b32_e32 v20, 13, v36
	v_mov_b32_e32 v21, v3
	v_lshlrev_b32_e32 v22, 12, v22
	v_mov_b32_e32 v23, v3
	v_lshlrev_b32_e32 v24, 12, v24
	v_mov_b32_e32 v25, v3
	v_lshlrev_b32_e32 v26, 12, v26
	v_mov_b32_e32 v27, v3
	v_lshlrev_b32_e32 v28, 12, v28
	v_mov_b32_e32 v29, v3
	v_lshlrev_b32_e32 v30, 12, v30
	v_mov_b32_e32 v31, v3
	v_lshlrev_b32_e32 v32, 12, v32
	v_mov_b32_e32 v33, v3
	v_lshlrev_b32_e32 v34, 12, v34
	v_mov_b32_e32 v35, v3
	v_lshlrev_b32_e32 v36, 12, v36
	v_mov_b32_e32 v37, v3
	s_lshl_b32 s16, s6, 5
	s_lshl_b32 s17, s8, 5
	s_lshl_b32 s18, s6, 1
	s_lshl_b32 s19, s8, 1
	s_mov_b32 s20, 0xb0000
	s_movk_i32 s21, 0x7fff
	s_mov_b32 s22, 0xffff0000
	s_mov_b32 s23, 0xb0c0
	s_mov_b32 s24, 0x58000
	s_mov_b32 s25, 0x109000
	s_mov_b32 s26, 0x161000
	s_mov_b32 s27, 0x1b9000
	s_mov_b32 s28, 0x212000
	s_mov_b32 s29, 0x26a000
	s_mov_b32 s30, 0x2c3000
	s_mov_b32 s31, 0x31b000
	s_mov_b32 s34, 0x373000
	s_mov_b32 s35, 0x3cc000
	s_mov_b32 s36, 0x424000
	s_mov_b32 s37, 0x47c000
	s_mov_b32 s38, 0x4d5000
	s_mov_b32 s39, 0x52d000
	v_lshlrev_b32_e32 v2, 2, v2
	v_add_u32_e32 v43, 0x420, v42
	v_add_u32_e32 v44, 0x428, v42
	v_add_u32_e32 v45, 0x840, v42
	v_add_u32_e32 v46, 0x848, v42
	v_add_u32_e32 v47, 0xc60, v42
	v_add_u32_e32 v48, 0xc68, v42
	v_add_u32_e32 v49, 0x1080, v42
	v_add_u32_e32 v50, 0x1088, v42
	v_add_u32_e32 v51, 0x14a0, v42
	v_add_u32_e32 v52, 0x14a8, v42
	s_mov_b32 s40, s6
	s_branch .Lwo_11

.Lwo_11:
	s_mov_b64 s[10:11], -1
	v_add_u32_e32 v72, 0x18c0, v42
	v_add_u32_e32 v73, 0x18c8, v42
	v_add_u32_e32 v68, 0x1ce0, v42
	v_add_u32_e32 v69, 0x1ce8, v42
	v_add_u32_e32 v70, 0x2100, v42
	v_add_u32_e32 v71, 0x2108, v42
	v_add_u32_e32 v54, 0x2520, v42
	v_add_u32_e32 v55, 0x2528, v42
	v_add_u32_e32 v56, 0x2940, v42
	v_add_u32_e32 v57, 0x2948, v42
	v_add_u32_e32 v58, 0x2d60, v42
	v_add_u32_e32 v59, 0x2d68, v42
	v_add_u32_e32 v60, 0x3180, v42
	v_add_u32_e32 v61, 0x3188, v42
	v_add_u32_e32 v62, 0x35a0, v42
	v_add_u32_e32 v63, 0x35a8, v42
	v_add_u32_e32 v64, 0x39c0, v42
	v_add_u32_e32 v65, 0x39c8, v42
	v_add_u32_e32 v66, 0x3de0, v42
	v_add_u32_e32 v67, 0x3de8, v42
	v_lshlrev_b32_e32 v38, 1, v4
	v_add_u32_e32 v53, 0x200, v5
	s_and_b32 s0, s18, 0x7fffff80
	s_add_i32 s10, s0, 0xffffd400
	v_or_b32_e32 v40, s10, v1
	v_mov_b32_e32 v41, v3
	v_readlane_b32 s44, v254, 12
	s_and_b32 s11, s16, 0x7e0
	v_lshlrev_b64 v[40:41], 13, v[40:41]
	v_readlane_b32 s52, v254, 20
	v_readlane_b32 s53, v254, 21
	s_lshl_b32 s0, s11, 2
	v_mov_b32_e32 v39, v3
	v_lshl_add_u64 v[40:41], s[52:53], 0, v[40:41]
	v_lshl_add_u64 v[40:41], v[40:41], 0, s[0:1]
	v_lshl_add_u64 v[40:41], v[40:41], 0, v[2:3]
	v_add_co_u32_e32 v78, vcc, 0x10000, v40
	s_lshl_b32 s0, s11, 13
	s_nop 0
	v_addc_co_u32_e32 v79, vcc, 0, v41, vcc
	v_add_co_u32_e32 v82, vcc, 0x20000, v40
	global_load_dwordx4 v[74:77], v[40:41], off
	s_nop 0
	global_load_dwordx4 v[78:81], v[78:79], off
	v_addc_co_u32_e32 v83, vcc, 0, v41, vcc
	v_add_co_u32_e32 v86, vcc, 0x30000, v40
	s_add_u32 s0, s14, s0
	s_nop 0
	v_addc_co_u32_e32 v87, vcc, 0, v41, vcc
	v_add_co_u32_e32 v90, vcc, 0x40000, v40
	global_load_dwordx4 v[82:85], v[82:83], off
	s_nop 0
	global_load_dwordx4 v[86:89], v[86:87], off
	v_addc_co_u32_e32 v91, vcc, 0, v41, vcc
	v_add_co_u32_e32 v94, vcc, 0x50000, v40
	s_mov_b32 s11, s1
	s_nop 0
	v_addc_co_u32_e32 v95, vcc, 0, v41, vcc
	v_add_co_u32_e32 v98, vcc, 0x60000, v40
	global_load_dwordx4 v[90:93], v[90:91], off
	s_nop 0
	global_load_dwordx4 v[94:97], v[94:95], off
	v_addc_co_u32_e32 v99, vcc, 0, v41, vcc
	v_add_co_u32_e32 v102, vcc, 0x70000, v40
	s_addc_u32 s12, s15, 0
	s_nop 0
	v_addc_co_u32_e32 v103, vcc, 0, v41, vcc
	v_add_co_u32_e32 v106, vcc, 0x80000, v40
	global_load_dwordx4 v[98:101], v[98:99], off
	s_nop 0
	global_load_dwordx4 v[102:105], v[102:103], off
	v_addc_co_u32_e32 v107, vcc, 0, v41, vcc
	v_add_co_u32_e32 v110, vcc, 0x90000, v40
	s_lshl_b64 s[10:11], s[10:11], 1
	s_nop 0
	v_addc_co_u32_e32 v111, vcc, 0, v41, vcc
	v_add_co_u32_e32 v114, vcc, 0xa0000, v40
	global_load_dwordx4 v[106:109], v[106:107], off
	s_nop 0
	global_load_dwordx4 v[110:113], v[110:111], off
	v_addc_co_u32_e32 v115, vcc, 0, v41, vcc
	v_add_co_u32_e32 v118, vcc, 0xb0000, v40
	s_add_u32 s10, s0, s10
	s_nop 0
	v_addc_co_u32_e32 v119, vcc, 0, v41, vcc
	v_add_co_u32_e32 v122, vcc, 0xc0000, v40
	global_load_dwordx4 v[114:117], v[114:115], off
	s_nop 0
	global_load_dwordx4 v[118:121], v[118:119], off
	v_addc_co_u32_e32 v123, vcc, 0, v41, vcc
	v_add_co_u32_e32 v126, vcc, 0xd0000, v40
	s_addc_u32 s11, s12, s11
	s_nop 0
	v_addc_co_u32_e32 v127, vcc, 0, v41, vcc
	global_load_dwordx4 v[122:125], v[122:123], off
	s_nop 0
	global_load_dwordx4 v[126:129], v[126:127], off
	v_add_co_u32_e32 v130, vcc, 0xe0000, v40
	v_readlane_b32 s45, v254, 13
	s_nop 0
	v_addc_co_u32_e32 v131, vcc, 0, v41, vcc
	v_add_co_u32_e32 v40, vcc, 0xf0000, v40
	global_load_dwordx4 v[130:133], v[130:131], off
	s_nop 0
	v_addc_co_u32_e32 v41, vcc, 0, v41, vcc
	global_load_dwordx4 v[134:137], v[40:41], off
	v_lshl_add_u64 v[40:41], s[10:11], 0, v[38:39]
	v_readlane_b32 s46, v254, 14
	v_readlane_b32 s47, v254, 15
	v_readlane_b32 s48, v254, 16
	v_readlane_b32 s49, v254, 17
	v_readlane_b32 s50, v254, 18
	v_readlane_b32 s51, v254, 19
	v_readlane_b32 s54, v254, 22
	v_readlane_b32 s55, v254, 23
	v_readlane_b32 s56, v254, 24
	v_readlane_b32 s57, v254, 25
	v_readlane_b32 s58, v254, 26
	v_readlane_b32 s59, v254, 27
	s_mov_b64 s[10:11], 0
	s_waitcnt vmcnt(15)
	ds_write2_b32 v42, v74, v75 offset1:1
	ds_write2_b32 v42, v76, v77 offset0:2 offset1:3
	s_waitcnt vmcnt(14)
	ds_write2_b32 v43, v78, v79 offset1:1
	ds_write2_b32 v44, v80, v81 offset1:1
	s_waitcnt vmcnt(13)
	ds_write2_b32 v45, v82, v83 offset1:1
	ds_write2_b32 v46, v84, v85 offset1:1
	s_waitcnt vmcnt(12)
	ds_write2_b32 v47, v86, v87 offset1:1
	ds_write2_b32 v48, v88, v89 offset1:1
	s_waitcnt vmcnt(11)
	ds_write2_b32 v49, v90, v91 offset1:1
	ds_write2_b32 v50, v92, v93 offset1:1
	s_waitcnt vmcnt(10)
	ds_write2_b32 v51, v94, v95 offset1:1
	ds_write2_b32 v52, v96, v97 offset1:1
	s_waitcnt vmcnt(9)
	ds_write2_b32 v72, v98, v99 offset1:1
	ds_write2_b32 v73, v100, v101 offset1:1
	s_waitcnt vmcnt(8)
	ds_write2_b32 v68, v102, v103 offset1:1
	ds_write2_b32 v69, v104, v105 offset1:1
	s_waitcnt vmcnt(7)
	ds_write2_b32 v70, v106, v107 offset1:1
	ds_write2_b32 v71, v108, v109 offset1:1
	s_waitcnt vmcnt(6)
	ds_write2_b32 v54, v110, v111 offset1:1
	ds_write2_b32 v55, v112, v113 offset1:1
	s_waitcnt vmcnt(5)
	ds_write2_b32 v56, v114, v115 offset1:1
	ds_write2_b32 v57, v116, v117 offset1:1
	s_waitcnt vmcnt(4)
	ds_write2_b32 v58, v118, v119 offset1:1
	ds_write2_b32 v59, v120, v121 offset1:1
	s_waitcnt vmcnt(3)
	ds_write2_b32 v60, v122, v123 offset1:1
	ds_write2_b32 v61, v124, v125 offset1:1
	s_waitcnt vmcnt(2)
	ds_write2_b32 v62, v126, v127 offset1:1
	ds_write2_b32 v63, v128, v129 offset1:1
	s_waitcnt vmcnt(1)
	ds_write2_b32 v64, v130, v131 offset1:1
	ds_write2_b32 v65, v132, v133 offset1:1
	s_waitcnt vmcnt(0)
	ds_write2_b32 v66, v134, v135 offset1:1
	ds_write2_b32 v67, v136, v137 offset1:1
	s_waitcnt lgkmcnt(0)
	ds_read2_b32 v[78:79], v5 offset1:4
	ds_read2_b32 v[80:81], v5 offset0:33 offset1:37
	ds_read2_b32 v[82:83], v5 offset0:66 offset1:70
	ds_read2_b32 v[84:85], v5 offset0:99 offset1:103
	ds_read2_b32 v[86:87], v5 offset0:132 offset1:136
	s_waitcnt lgkmcnt(4)
	v_bfe_u32 v39, v78, 16, 1
	v_add3_u32 v39, v78, v39, s21
	s_waitcnt lgkmcnt(3)
	v_bfe_u32 v74, v80, 16, 1
	v_lshrrev_b32_e32 v39, 16, v39
	v_add3_u32 v74, v80, v74, s21
	ds_read2_b32 v[88:89], v5 offset0:165 offset1:169
	v_and_or_b32 v74, v74, s22, v39
	s_waitcnt lgkmcnt(3)
	v_bfe_u32 v39, v82, 16, 1
	v_add3_u32 v39, v82, v39, s21
	s_waitcnt lgkmcnt(2)
	v_bfe_u32 v75, v84, 16, 1
	ds_read2_b32 v[90:91], v5 offset0:198 offset1:202
	v_lshrrev_b32_e32 v39, 16, v39
	v_add3_u32 v75, v84, v75, s21
	ds_read2_b32 v[92:93], v5 offset0:231 offset1:235
	v_and_or_b32 v75, v75, s22, v39
	s_waitcnt lgkmcnt(3)
	v_bfe_u32 v39, v86, 16, 1
	v_add3_u32 v39, v86, v39, s21
	s_waitcnt lgkmcnt(2)
	v_bfe_u32 v76, v88, 16, 1
	v_lshrrev_b32_e32 v39, 16, v39
	v_add3_u32 v76, v88, v76, s21
	v_and_or_b32 v76, v76, s22, v39
	s_waitcnt lgkmcnt(1)
	v_bfe_u32 v39, v90, 16, 1
	v_add3_u32 v39, v90, v39, s21
	s_waitcnt lgkmcnt(0)
	v_bfe_u32 v77, v92, 16, 1
	v_lshrrev_b32_e32 v39, 16, v39
	v_add3_u32 v77, v92, v77, s21
	v_and_or_b32 v77, v77, s22, v39
	v_lshl_add_u64 v[94:95], v[40:41], 0, v[6:7]
	v_bfe_u32 v39, v79, 16, 1
	global_store_dwordx4 v[94:95], v[74:77], off
	v_add3_u32 v39, v79, v39, s21
	v_lshrrev_b32_e32 v39, 16, v39
	v_bfe_u32 v74, v81, 16, 1
	v_add3_u32 v74, v81, v74, s21
	v_and_or_b32 v74, v74, s22, v39
	v_bfe_u32 v39, v83, 16, 1
	v_add3_u32 v39, v83, v39, s21
	v_bfe_u32 v75, v85, 16, 1
	v_lshrrev_b32_e32 v39, 16, v39
	v_add3_u32 v75, v85, v75, s21
	v_and_or_b32 v75, v75, s22, v39
	v_bfe_u32 v39, v87, 16, 1
	v_add3_u32 v39, v87, v39, s21
	v_bfe_u32 v76, v89, 16, 1
	v_lshrrev_b32_e32 v39, 16, v39
	v_add3_u32 v76, v89, v76, s21
	v_and_or_b32 v76, v76, s22, v39
	v_bfe_u32 v39, v91, 16, 1
	v_add3_u32 v39, v91, v39, s21
	v_bfe_u32 v77, v93, 16, 1
	v_lshrrev_b32_e32 v39, 16, v39
	v_add3_u32 v77, v93, v77, s21
	ds_read2_b32 v[78:79], v5 offset0:8 offset1:12
	v_and_or_b32 v77, v77, s22, v39
	v_lshl_add_u64 v[80:81], v[40:41], 0, v[8:9]
	global_store_dwordx4 v[80:81], v[74:77], off
	ds_read2_b32 v[80:81], v5 offset0:41 offset1:45
	ds_read2_b32 v[82:83], v5 offset0:74 offset1:78
	ds_read2_b32 v[84:85], v5 offset0:107 offset1:111
	s_waitcnt lgkmcnt(3)
	v_bfe_u32 v39, v78, 16, 1
	v_add3_u32 v39, v78, v39, s21
	s_waitcnt lgkmcnt(2)
	v_bfe_u32 v74, v80, 16, 1
	ds_read2_b32 v[86:87], v5 offset0:140 offset1:144
	v_lshrrev_b32_e32 v39, 16, v39
	v_add3_u32 v74, v80, v74, s21
	ds_read2_b32 v[88:89], v5 offset0:173 offset1:177
	v_and_or_b32 v74, v74, s22, v39
	s_waitcnt lgkmcnt(3)
	v_bfe_u32 v39, v82, 16, 1
	v_add3_u32 v39, v82, v39, s21
	s_waitcnt lgkmcnt(2)
	v_bfe_u32 v75, v84, 16, 1
	ds_read2_b32 v[90:91], v5 offset0:206 offset1:210
	v_lshrrev_b32_e32 v39, 16, v39
	v_add3_u32 v75, v84, v75, s21
	ds_read2_b32 v[92:93], v5 offset0:239 offset1:243
	v_and_or_b32 v75, v75, s22, v39
	s_waitcnt lgkmcnt(3)
	v_bfe_u32 v39, v86, 16, 1
	v_add3_u32 v39, v86, v39, s21
	s_waitcnt lgkmcnt(2)
	v_bfe_u32 v76, v88, 16, 1
	v_lshrrev_b32_e32 v39, 16, v39
	v_add3_u32 v76, v88, v76, s21
	v_and_or_b32 v76, v76, s22, v39
	s_waitcnt lgkmcnt(1)
	v_bfe_u32 v39, v90, 16, 1
	v_add3_u32 v39, v90, v39, s21
	s_waitcnt lgkmcnt(0)
	v_bfe_u32 v77, v92, 16, 1
	v_lshrrev_b32_e32 v39, 16, v39
	v_add3_u32 v77, v92, v77, s21
	v_and_or_b32 v77, v77, s22, v39
	v_lshl_add_u64 v[94:95], v[40:41], 0, v[10:11]
	v_bfe_u32 v39, v79, 16, 1
	global_store_dwordx4 v[94:95], v[74:77], off
	v_add3_u32 v39, v79, v39, s21
	v_lshrrev_b32_e32 v39, 16, v39
	v_bfe_u32 v74, v81, 16, 1
	v_add3_u32 v74, v81, v74, s21
	v_and_or_b32 v74, v74, s22, v39
	v_bfe_u32 v39, v83, 16, 1
	v_add3_u32 v39, v83, v39, s21
	v_bfe_u32 v75, v85, 16, 1
	v_lshrrev_b32_e32 v39, 16, v39
	v_add3_u32 v75, v85, v75, s21
	v_and_or_b32 v75, v75, s22, v39
	v_bfe_u32 v39, v87, 16, 1
	v_add3_u32 v39, v87, v39, s21
	v_bfe_u32 v76, v89, 16, 1
	v_lshrrev_b32_e32 v39, 16, v39
	v_add3_u32 v76, v89, v76, s21
	v_and_or_b32 v76, v76, s22, v39
	v_bfe_u32 v39, v91, 16, 1
	v_add3_u32 v39, v91, v39, s21
	v_bfe_u32 v77, v93, 16, 1
	v_lshrrev_b32_e32 v39, 16, v39
	v_add3_u32 v77, v93, v77, s21
	ds_read2_b32 v[78:79], v5 offset0:16 offset1:20
	v_and_or_b32 v77, v77, s22, v39
	v_lshl_add_u64 v[80:81], v[40:41], 0, v[12:13]
	global_store_dwordx4 v[80:81], v[74:77], off
	ds_read2_b32 v[80:81], v5 offset0:49 offset1:53
	ds_read2_b32 v[82:83], v5 offset0:82 offset1:86
	ds_read2_b32 v[84:85], v5 offset0:115 offset1:119
	s_waitcnt lgkmcnt(3)
	v_bfe_u32 v39, v78, 16, 1
	v_add3_u32 v39, v78, v39, s21
	s_waitcnt lgkmcnt(2)
	v_bfe_u32 v74, v80, 16, 1
	ds_read2_b32 v[86:87], v5 offset0:148 offset1:152
	v_lshrrev_b32_e32 v39, 16, v39
	v_add3_u32 v74, v80, v74, s21
	ds_read2_b32 v[88:89], v5 offset0:181 offset1:185
	v_and_or_b32 v74, v74, s22, v39
	s_waitcnt lgkmcnt(3)
	v_bfe_u32 v39, v82, 16, 1
	v_add3_u32 v39, v82, v39, s21
	s_waitcnt lgkmcnt(2)
	v_bfe_u32 v75, v84, 16, 1
	ds_read2_b32 v[90:91], v5 offset0:214 offset1:218
	v_lshrrev_b32_e32 v39, 16, v39
	v_add3_u32 v75, v84, v75, s21
	ds_read2_b32 v[92:93], v5 offset0:247 offset1:251
	v_and_or_b32 v75, v75, s22, v39
	s_waitcnt lgkmcnt(3)
	v_bfe_u32 v39, v86, 16, 1
	v_add3_u32 v39, v86, v39, s21
	s_waitcnt lgkmcnt(2)
	v_bfe_u32 v76, v88, 16, 1
	v_lshrrev_b32_e32 v39, 16, v39
	v_add3_u32 v76, v88, v76, s21
	v_and_or_b32 v76, v76, s22, v39
	s_waitcnt lgkmcnt(1)
	v_bfe_u32 v39, v90, 16, 1
	v_add3_u32 v39, v90, v39, s21
	s_waitcnt lgkmcnt(0)
	v_bfe_u32 v77, v92, 16, 1
	v_lshrrev_b32_e32 v39, 16, v39
	v_add3_u32 v77, v92, v77, s21
	v_and_or_b32 v77, v77, s22, v39
	v_lshl_add_u64 v[94:95], v[40:41], 0, v[14:15]
	v_bfe_u32 v39, v79, 16, 1
	global_store_dwordx4 v[94:95], v[74:77], off
	v_add3_u32 v39, v79, v39, s21
	v_lshrrev_b32_e32 v39, 16, v39
	v_bfe_u32 v74, v81, 16, 1
	v_add3_u32 v74, v81, v74, s21
	v_and_or_b32 v74, v74, s22, v39
	v_bfe_u32 v39, v83, 16, 1
	v_add3_u32 v39, v83, v39, s21
	v_bfe_u32 v75, v85, 16, 1
	v_lshrrev_b32_e32 v39, 16, v39
	v_add3_u32 v75, v85, v75, s21
	v_and_or_b32 v75, v75, s22, v39
	v_bfe_u32 v39, v87, 16, 1
	v_add3_u32 v39, v87, v39, s21
	v_bfe_u32 v76, v89, 16, 1
	v_lshrrev_b32_e32 v39, 16, v39
	v_add3_u32 v76, v89, v76, s21
	v_and_or_b32 v76, v76, s22, v39
	v_bfe_u32 v39, v91, 16, 1
	v_add3_u32 v39, v91, v39, s21
	v_bfe_u32 v77, v93, 16, 1
	v_lshrrev_b32_e32 v39, 16, v39
	v_add3_u32 v77, v93, v77, s21
	ds_read2_b32 v[78:79], v5 offset0:24 offset1:28
	v_and_or_b32 v77, v77, s22, v39
	v_lshl_add_u64 v[80:81], v[40:41], 0, v[16:17]
	global_store_dwordx4 v[80:81], v[74:77], off
	ds_read2_b32 v[80:81], v5 offset0:57 offset1:61
	ds_read2_b32 v[82:83], v5 offset0:90 offset1:94
	ds_read2_b32 v[84:85], v5 offset0:123 offset1:127
	s_waitcnt lgkmcnt(3)
	v_bfe_u32 v39, v78, 16, 1
	v_add3_u32 v39, v78, v39, s21
	s_waitcnt lgkmcnt(2)
	v_bfe_u32 v74, v80, 16, 1
	ds_read2_b32 v[86:87], v5 offset0:156 offset1:160
	v_lshrrev_b32_e32 v39, 16, v39
	v_add3_u32 v74, v80, v74, s21
	ds_read2_b32 v[88:89], v5 offset0:189 offset1:193
	v_and_or_b32 v74, v74, s22, v39
	s_waitcnt lgkmcnt(3)
	v_bfe_u32 v39, v82, 16, 1
	v_add3_u32 v39, v82, v39, s21
	s_waitcnt lgkmcnt(2)
	v_bfe_u32 v75, v84, 16, 1
	ds_read2_b32 v[90:91], v5 offset0:222 offset1:226
	v_lshrrev_b32_e32 v39, 16, v39
	v_add3_u32 v75, v84, v75, s21
	ds_read2_b32 v[92:93], v53 offset0:127 offset1:131
	v_and_or_b32 v75, v75, s22, v39
	s_waitcnt lgkmcnt(3)
	v_bfe_u32 v39, v86, 16, 1
	v_add3_u32 v39, v86, v39, s21
	s_waitcnt lgkmcnt(2)
	v_bfe_u32 v76, v88, 16, 1
	v_lshrrev_b32_e32 v39, 16, v39
	v_add3_u32 v76, v88, v76, s21
	v_and_or_b32 v76, v76, s22, v39
	s_waitcnt lgkmcnt(1)
	v_bfe_u32 v39, v90, 16, 1
	v_add3_u32 v39, v90, v39, s21
	s_waitcnt lgkmcnt(0)
	v_bfe_u32 v77, v92, 16, 1
	v_lshrrev_b32_e32 v39, 16, v39
	v_add3_u32 v77, v92, v77, s21
	v_and_or_b32 v77, v77, s22, v39
	v_lshl_add_u64 v[94:95], v[40:41], 0, v[18:19]
	v_bfe_u32 v39, v79, 16, 1
	global_store_dwordx4 v[94:95], v[74:77], off
	v_add3_u32 v39, v79, v39, s21
	v_lshrrev_b32_e32 v39, 16, v39
	v_bfe_u32 v74, v81, 16, 1
	v_add3_u32 v74, v81, v74, s21
	v_and_or_b32 v74, v74, s22, v39
	v_bfe_u32 v39, v83, 16, 1
	v_add3_u32 v39, v83, v39, s21
	v_bfe_u32 v75, v85, 16, 1
	v_lshrrev_b32_e32 v39, 16, v39
	v_add3_u32 v75, v85, v75, s21
	v_and_or_b32 v75, v75, s22, v39
	v_bfe_u32 v39, v87, 16, 1
	v_add3_u32 v39, v87, v39, s21
	v_bfe_u32 v76, v89, 16, 1
	v_lshrrev_b32_e32 v39, 16, v39
	v_add3_u32 v76, v89, v76, s21
	v_and_or_b32 v76, v76, s22, v39
	v_bfe_u32 v39, v91, 16, 1
	v_add3_u32 v39, v91, v39, s21
	v_bfe_u32 v77, v93, 16, 1
	v_lshrrev_b32_e32 v39, 16, v39
	v_add3_u32 v77, v93, v77, s21
	v_and_or_b32 v77, v77, s22, v39
	v_lshl_add_u64 v[40:41], v[40:41], 0, v[20:21]
	global_store_dwordx4 v[40:41], v[74:77], off
	s_waitcnt lgkmcnt(0)
	s_branch .Lwo_10
.Lwo_done:
	s_nop 0
	v_readlane_b32 s16, v253, 0
	v_readlane_b32 s17, v253, 1
	v_readlane_b32 s18, v253, 2
	v_readlane_b32 s19, v253, 3
	v_readlane_b32 s20, v253, 4
	v_readlane_b32 s21, v253, 5
	v_readlane_b32 s22, v253, 6
	v_readlane_b32 s23, v253, 7
	v_readlane_b32 s24, v253, 8
	v_readlane_b32 s25, v253, 9
	v_readlane_b32 s26, v253, 10
	v_readlane_b32 s27, v253, 11
	v_readlane_b32 s28, v253, 12
	v_readlane_b32 s29, v253, 13
	v_readlane_b32 s30, v253, 14
	v_readlane_b32 s31, v253, 15
	v_readlane_b32 s32, v253, 16
	v_readlane_b32 s33, v253, 17
	v_readlane_b32 s34, v253, 18
	v_readlane_b32 s35, v253, 19
	v_readlane_b32 s36, v253, 20
	v_readlane_b32 s37, v253, 21
	v_readlane_b32 s38, v253, 22
	v_readlane_b32 s39, v253, 23
	v_readlane_b32 s40, v253, 24
	v_readlane_b32 s41, v253, 25

	.amdhsa_kernel _Z9hymba_fwd4Args
		.amdhsa_group_segment_fixed_size 0
		.amdhsa_private_segment_fixed_size 0
		.amdhsa_kernarg_size 456
		.amdhsa_user_sgpr_count 2
		.amdhsa_user_sgpr_dispatch_ptr 0
		.amdhsa_user_sgpr_queue_ptr 0
		.amdhsa_user_sgpr_kernarg_segment_ptr 1
		.amdhsa_user_sgpr_dispatch_id 0
		.amdhsa_user_sgpr_kernarg_preload_length 0
		.amdhsa_user_sgpr_kernarg_preload_offset 0
		.amdhsa_user_sgpr_private_segment_size 0
		.amdhsa_uses_dynamic_stack 0
		.amdhsa_enable_private_segment 0
		.amdhsa_system_sgpr_workgroup_id_x 1
		.amdhsa_system_sgpr_workgroup_id_y 0
		.amdhsa_system_sgpr_workgroup_id_z 0
		.amdhsa_system_sgpr_workgroup_info 0
		.amdhsa_system_vgpr_workitem_id 0
		.amdhsa_next_free_vgpr 255
		.amdhsa_next_free_sgpr 100
		.amdhsa_accum_offset 256
		.amdhsa_reserve_vcc 1
		.amdhsa_float_round_mode_32 0
		.amdhsa_float_round_mode_16_64 0
		.amdhsa_float_denorm_mode_32 3
		.amdhsa_float_denorm_mode_16_64 3
		.amdhsa_dx10_clamp 1
		.amdhsa_ieee_mode 1
		.amdhsa_fp16_overflow 0
		.amdhsa_tg_split 0
		.amdhsa_exception_fp_ieee_invalid_op 0
		.amdhsa_exception_fp_denorm_src 0
		.amdhsa_exception_fp_ieee_div_zero 0
		.amdhsa_exception_fp_ieee_overflow 0
		.amdhsa_exception_fp_ieee_underflow 0
		.amdhsa_exception_fp_ieee_inexact 0
		.amdhsa_exception_int_div_zero 0
	.end_amdhsa_kernel

amdhsa.kernels:
  - .agpr_count:     0
    .args:
      - .offset:         0
        .size:           200
        .value_kind:     by_value
      - .offset:         200
        .size:           4
        .value_kind:     hidden_block_count_x
      - .offset:         204
        .size:           4
        .value_kind:     hidden_block_count_y
      - .offset:         208
        .size:           4
        .value_kind:     hidden_block_count_z
      - .offset:         212
        .size:           2
        .value_kind:     hidden_group_size_x
      - .offset:         214
        .size:           2
        .value_kind:     hidden_group_size_y
      - .offset:         216
        .size:           2
        .value_kind:     hidden_group_size_z
      - .offset:         218
        .size:           2
        .value_kind:     hidden_remainder_x
      - .offset:         220
        .size:           2
        .value_kind:     hidden_remainder_y
      - .offset:         222
        .size:           2
        .value_kind:     hidden_remainder_z
      - .offset:         240
        .size:           8
        .value_kind:     hidden_global_offset_x
      - .offset:         248
        .size:           8
        .value_kind:     hidden_global_offset_y
      - .offset:         256
        .size:           8
        .value_kind:     hidden_global_offset_z
      - .offset:         264
        .size:           2
        .value_kind:     hidden_grid_dims
      - .offset:         320
        .size:           4
        .value_kind:     hidden_dynamic_lds_size
    .group_segment_fixed_size: 0
    .kernarg_segment_align: 8
    .kernarg_segment_size: 456
    .language:       OpenCL C
    .language_version:
      - 2
      - 0
    .max_flat_workgroup_size: 512
    .name:           _Z9hymba_fwd4Args
    .private_segment_fixed_size: 0
    .sgpr_count:     106
    .sgpr_spill_count: 71
    .symbol:         _Z9hymba_fwd4Args.kd
    .uniform_work_group_size: 1
    .uses_dynamic_stack: false
    .vgpr_count:     255
    .vgpr_spill_count: 0
    .wavefront_size: 64
